# attention ping-pong loops: static s_setprio 1 for the early (first-on-SIMD) waves instead of the late ones
# baseline (speedup 1.0000x reference)
.LBB0_292:
	v_add_u32_e32 v2, v2, v3
	v_add_u32_e32 v2, v2, v5
	v_add_u32_e32 v2, v2, v4
	v_add_u32_e32 v2, v2, v7
	v_add_u32_e32 v2, v2, v6
	v_add_u32_e32 v2, v2, v9
	v_or_b32_e32 v2, v8, v2
	v_cmp_ne_u32_e32 vcc, 0, v2
	s_and_b64 s[0:1], s[30:31], exec
	s_cselect_b32 s50, 16, 0
	v_cndmask_b32_e64 v2, 0, 1, vcc
	s_mov_b32 s5, s81
	v_readfirstlane_b32 s0, v2
	s_bitcmp1_b32 s0, 0
	s_cselect_b64 s[10:11], -1, 0
	s_xor_b64 s[38:39], s[10:11], -1
	s_lshl_b64 s[0:1], s[4:5], 2
	v_readlane_b32 s2, v254, 42
	s_add_u32 s24, s2, s0
	v_readlane_b32 s2, v254, 43
	s_addc_u32 s25, s2, s1
	s_or_b32 s33, s50, 0x400
	s_barrier
	s_cmp_lg_u64 s[10:11], 0
	s_cbranch_scc1 .Lprio_skip
	s_setprio 1
